# baseline (speedup 1.0000x reference)
.Lrs_a_4:
	s_add_u32 s81, s40, s22
	s_addc_u32 s82, s41, s23
	s_add_u32 s29, s40, 0x100
	s_addc_u32 s44, s41, 0
	s_and_b64 s[42:43], s[14:15], exec
	ds_read_b128 v[82:85], v161
	ds_read_b128 v[94:97], v161 offset:2048
	ds_read_b128 v[102:105], v162
	ds_read_b128 v[110:113], v162 offset:2048
	s_cselect_b32 s47, s37, s44
	s_cselect_b32 s46, s36, s29
	s_add_u32 s29, s38, 0x100
	s_addc_u32 s44, s39, 0
	s_and_b64 s[42:43], s[14:15], exec
	s_cselect_b32 s49, s5, s44
	s_cselect_b32 s48, s4, s29
	s_add_u32 s44, s46, 0x80
	s_addc_u32 s45, s47, 0
	s_add_u32 s42, s48, 0x80
	s_addc_u32 s43, s49, 0
	ds_read_b128 v[58:61], v163
	ds_read_b128 v[66:69], v163 offset:2048
	ds_read_b128 v[62:65], v164
	ds_read_b128 v[70:73], v164 offset:2048
	ds_read_b128 v[74:77], v163 offset:4096
	ds_read_b128 v[86:89], v163 offset:6144
	ds_read_b128 v[78:81], v164 offset:4096
	ds_read_b128 v[90:93], v164 offset:6144
	s_add_u32 s78, s81, 0x80
	s_addc_u32 s79, s82, 0
	s_mov_b32 m0, s70
	s_nop 0
	global_load_lds_dwordx4 v146, s[78:79]
	s_mov_b32 m0, s71
	s_nop 0
	global_load_lds_dwordx4 v150, s[78:79]
	s_waitcnt lgkmcnt(8)
	ds_read_b128 v[142:145], v161 offset:16384
	ds_read_b128 v[166:169], v161 offset:18432
	ds_read_b128 v[170:173], v162 offset:16384
	ds_read_b128 v[174:177], v162 offset:18432
	s_waitcnt vmcnt(16)
	v_mov_b32_e32 v1, v0
	v_pk_mul_f32 v[16:17], v[0:1], v[16:17]
	v_pk_mul_f32 v[14:15], v[154:155], v[14:15]
	v_pk_mul_f32 v[12:13], v[0:1], v[12:13]
	v_pk_mul_f32 v[10:11], v[154:155], v[10:11]
	v_pk_mul_f32 v[8:9], v[0:1], v[8:9]
	v_pk_mul_f32 v[6:7], v[154:155], v[6:7]
	v_pk_mul_f32 v[4:5], v[0:1], v[4:5]
	v_pk_mul_f32 v[2:3], v[154:155], v[2:3]
	s_waitcnt vmcnt(8)
	s_waitcnt lgkmcnt(0)
	s_barrier
	s_waitcnt lgkmcnt(0)
	s_setprio 1
	v_mfma_f32_16x16x128_f8f6f4 v[18:21], v[82:85], v[58:61], v[14:17] cbsz:4 blgp:4
	v_mfma_f32_16x16x128_f8f6f4 v[18:21], v[102:105], v[62:65], v[18:21] cbsz:4 blgp:4
	v_mfma_f32_16x16x128_f8f6f4 v[22:25], v[94:97], v[58:61], v[10:13] cbsz:4 blgp:4
	v_mfma_f32_16x16x128_f8f6f4 v[22:25], v[110:113], v[62:65], v[22:25] cbsz:4 blgp:4
	v_mfma_f32_16x16x128_f8f6f4 v[50:53], v[142:145], v[58:61], v[6:9] cbsz:4 blgp:4
	v_mfma_f32_16x16x128_f8f6f4 v[50:53], v[170:173], v[62:65], v[50:53] cbsz:4 blgp:4
	v_mfma_f32_16x16x128_f8f6f4 v[54:57], v[166:169], v[58:61], v[2:5] cbsz:4 blgp:4
	v_mfma_f32_16x16x128_f8f6f4 v[54:57], v[174:177], v[62:65], v[54:57] cbsz:4 blgp:4
	v_mfma_f32_16x16x128_f8f6f4 v[26:29], v[82:85], v[66:69], v[14:17] cbsz:4 blgp:4
	v_mfma_f32_16x16x128_f8f6f4 v[26:29], v[102:105], v[70:73], v[26:29] cbsz:4 blgp:4
	v_mfma_f32_16x16x128_f8f6f4 v[30:33], v[94:97], v[66:69], v[10:13] cbsz:4 blgp:4
	v_mfma_f32_16x16x128_f8f6f4 v[30:33], v[110:113], v[70:73], v[30:33] cbsz:4 blgp:4
	v_mfma_f32_16x16x128_f8f6f4 v[58:61], v[142:145], v[66:69], v[6:9] cbsz:4 blgp:4
	v_mfma_f32_16x16x128_f8f6f4 v[58:61], v[170:173], v[70:73], v[58:61] cbsz:4 blgp:4
	v_mfma_f32_16x16x128_f8f6f4 v[62:65], v[166:169], v[66:69], v[2:5] cbsz:4 blgp:4
	v_mfma_f32_16x16x128_f8f6f4 v[62:65], v[174:177], v[70:73], v[62:65] cbsz:4 blgp:4
	v_mfma_f32_16x16x128_f8f6f4 v[34:37], v[82:85], v[74:77], v[14:17] cbsz:4 blgp:4
	v_mfma_f32_16x16x128_f8f6f4 v[34:37], v[102:105], v[78:81], v[34:37] cbsz:4 blgp:4
	v_mfma_f32_16x16x128_f8f6f4 v[38:41], v[94:97], v[74:77], v[10:13] cbsz:4 blgp:4
	v_mfma_f32_16x16x128_f8f6f4 v[38:41], v[110:113], v[78:81], v[38:41] cbsz:4 blgp:4
	v_mfma_f32_16x16x128_f8f6f4 v[66:69], v[142:145], v[74:77], v[6:9] cbsz:4 blgp:4
	v_mfma_f32_16x16x128_f8f6f4 v[66:69], v[170:173], v[78:81], v[66:69] cbsz:4 blgp:4
	v_mfma_f32_16x16x128_f8f6f4 v[70:73], v[166:169], v[74:77], v[2:5] cbsz:4 blgp:4
	v_mfma_f32_16x16x128_f8f6f4 v[70:73], v[174:177], v[78:81], v[70:73] cbsz:4 blgp:4
	v_mfma_f32_16x16x128_f8f6f4 v[42:45], v[82:85], v[86:89], v[14:17] cbsz:4 blgp:4
	v_mfma_f32_16x16x128_f8f6f4 v[42:45], v[102:105], v[90:93], v[42:45] cbsz:4 blgp:4
	v_mfma_f32_16x16x128_f8f6f4 v[46:49], v[94:97], v[86:89], v[10:13] cbsz:4 blgp:4
	v_mfma_f32_16x16x128_f8f6f4 v[46:49], v[110:113], v[90:93], v[46:49] cbsz:4 blgp:4
	v_mfma_f32_16x16x128_f8f6f4 v[74:77], v[142:145], v[86:89], v[6:9] cbsz:4 blgp:4
	v_mfma_f32_16x16x128_f8f6f4 v[74:77], v[170:173], v[90:93], v[74:77] cbsz:4 blgp:4
	v_mfma_f32_16x16x128_f8f6f4 v[78:81], v[166:169], v[86:89], v[2:5] cbsz:4 blgp:4
	v_mfma_f32_16x16x128_f8f6f4 v[78:81], v[174:177], v[90:93], v[78:81] cbsz:4 blgp:4
	s_setprio 0
	s_barrier
	s_mov_b32 m0, s55
	s_nop 0
	global_load_lds_dwordx4 v148, s[48:49]
	s_mov_b32 m0, s56
	s_nop 0
	global_load_lds_dwordx4 v152, s[48:49]
	ds_read_b128 v[114:117], v163 offset:16384
	ds_read_b128 v[122:125], v163 offset:18432
	ds_read_b128 v[130:133], v164 offset:16384
	ds_read_b128 v[134:137], v164 offset:18432
	ds_read_b128 v[178:181], v163 offset:20480
	ds_read_b128 v[182:185], v163 offset:22528
	ds_read_b128 v[186:189], v164 offset:20480
	ds_read_b128 v[190:193], v164 offset:22528
	s_mov_b32 m0, s54
	s_nop 0
	global_load_lds_dwordx4 v146, s[46:47]
	s_mov_b32 m0, s57
	s_nop 0
	global_load_lds_dwordx4 v150, s[46:47]
	s_add_u32 s48, s48, s24
	s_addc_u32 s49, s49, s25
	s_mov_b32 m0, s58
	s_nop 0
	global_load_lds_dwordx4 v148, s[48:49]
	s_mov_b32 m0, s59
	s_nop 0
	global_load_lds_dwordx4 v152, s[48:49]
	s_waitcnt vmcnt(8)
	s_waitcnt lgkmcnt(0)
	s_barrier
	s_setprio 1
	v_mfma_f32_16x16x128_f8f6f4 v[86:89], v[82:85], v[114:117], v[14:17] cbsz:4 blgp:4
	v_mfma_f32_16x16x128_f8f6f4 v[86:89], v[102:105], v[130:133], v[86:89] cbsz:4 blgp:4
	v_mfma_f32_16x16x128_f8f6f4 v[90:93], v[94:97], v[114:117], v[10:13] cbsz:4 blgp:4
	v_mfma_f32_16x16x128_f8f6f4 v[90:93], v[110:113], v[130:133], v[90:93] cbsz:4 blgp:4
	v_mfma_f32_16x16x128_f8f6f4 v[98:101], v[82:85], v[122:125], v[14:17] cbsz:4 blgp:4
	v_mfma_f32_16x16x128_f8f6f4 v[98:101], v[102:105], v[134:137], v[98:101] cbsz:4 blgp:4
	v_mfma_f32_16x16x128_f8f6f4 v[106:109], v[94:97], v[122:125], v[10:13] cbsz:4 blgp:4
	v_mfma_f32_16x16x128_f8f6f4 v[106:109], v[110:113], v[134:137], v[106:109] cbsz:4 blgp:4
	v_mfma_f32_16x16x128_f8f6f4 v[118:121], v[82:85], v[178:181], v[14:17] cbsz:4 blgp:4
	v_mfma_f32_16x16x128_f8f6f4 v[118:121], v[102:105], v[186:189], v[118:121] cbsz:4 blgp:4
	v_mfma_f32_16x16x128_f8f6f4 v[126:129], v[94:97], v[178:181], v[10:13] cbsz:4 blgp:4
	v_mfma_f32_16x16x128_f8f6f4 v[126:129], v[110:113], v[186:189], v[126:129] cbsz:4 blgp:4
	v_mfma_f32_16x16x128_f8f6f4 v[138:141], v[82:85], v[182:185], v[14:17] cbsz:4 blgp:4
	v_mfma_f32_16x16x128_f8f6f4 v[138:141], v[102:105], v[190:193], v[138:141] cbsz:4 blgp:4
	v_mfma_f32_16x16x128_f8f6f4 v[82:85], v[94:97], v[182:185], v[10:13] cbsz:4 blgp:4
	v_mfma_f32_16x16x128_f8f6f4 v[82:85], v[110:113], v[190:193], v[82:85] cbsz:4 blgp:4
	v_mfma_f32_16x16x128_f8f6f4 v[94:97], v[142:145], v[114:117], v[6:9] cbsz:4 blgp:4
	v_mfma_f32_16x16x128_f8f6f4 v[94:97], v[170:173], v[130:133], v[94:97] cbsz:4 blgp:4
	v_mfma_f32_16x16x128_f8f6f4 v[102:105], v[166:169], v[114:117], v[2:5] cbsz:4 blgp:4
	v_mfma_f32_16x16x128_f8f6f4 v[102:105], v[174:177], v[130:133], v[102:105] cbsz:4 blgp:4
	v_mfma_f32_16x16x128_f8f6f4 v[110:113], v[142:145], v[122:125], v[6:9] cbsz:4 blgp:4
	v_mfma_f32_16x16x128_f8f6f4 v[110:113], v[170:173], v[134:137], v[110:113] cbsz:4 blgp:4
	v_mfma_f32_16x16x128_f8f6f4 v[114:117], v[166:169], v[122:125], v[2:5] cbsz:4 blgp:4
	v_mfma_f32_16x16x128_f8f6f4 v[114:117], v[174:177], v[134:137], v[114:117] cbsz:4 blgp:4
	v_mfma_f32_16x16x128_f8f6f4 v[122:125], v[142:145], v[178:181], v[6:9] cbsz:4 blgp:4
	v_mfma_f32_16x16x128_f8f6f4 v[122:125], v[170:173], v[186:189], v[122:125] cbsz:4 blgp:4
	v_mfma_f32_16x16x128_f8f6f4 v[130:133], v[166:169], v[178:181], v[2:5] cbsz:4 blgp:4
	v_mfma_f32_16x16x128_f8f6f4 v[130:133], v[174:177], v[186:189], v[130:133] cbsz:4 blgp:4
	v_mfma_f32_16x16x128_f8f6f4 v[134:137], v[142:145], v[182:185], v[6:9] cbsz:4 blgp:4
	v_mfma_f32_16x16x128_f8f6f4 v[134:137], v[170:173], v[190:193], v[134:137] cbsz:4 blgp:4
	v_mfma_f32_16x16x128_f8f6f4 v[142:145], v[166:169], v[182:185], v[2:5] cbsz:4 blgp:4
	v_mfma_f32_16x16x128_f8f6f4 v[142:145], v[174:177], v[190:193], v[142:145] cbsz:4 blgp:4
	s_setprio 0
	s_barrier
	ds_read_b128 v[166:169], v161 offset:32768
	ds_read_b128 v[170:173], v161 offset:34816
	ds_read_b128 v[174:177], v162 offset:32768
	ds_read_b128 v[178:181], v162 offset:34816
	ds_read_b128 v[182:185], v163 offset:32768
	ds_read_b128 v[186:189], v163 offset:34816
	ds_read_b128 v[190:193], v164 offset:32768
	ds_read_b128 v[194:197], v164 offset:34816
	ds_read_b128 v[198:201], v163 offset:36864
	ds_read_b128 v[202:205], v163 offset:38912
	ds_read_b128 v[206:209], v164 offset:36864
	ds_read_b128 v[210:213], v164 offset:38912
	s_add_u32 s46, s46, s22
	s_addc_u32 s47, s47, s23
	s_mov_b32 m0, s60
	s_nop 0
	global_load_lds_dwordx4 v146, s[46:47]
	s_mov_b32 m0, s61
	s_nop 0
	global_load_lds_dwordx4 v150, s[46:47]
	s_waitcnt lgkmcnt(8)
	ds_read_b128 v[214:217], v161 offset:49152
	ds_read_b128 v[218:221], v161 offset:51200
	ds_read_b128 v[222:225], v162 offset:49152
	ds_read_b128 v[226:229], v162 offset:51200
	s_waitcnt vmcnt(8)
	s_waitcnt lgkmcnt(0)
	s_barrier
	s_waitcnt lgkmcnt(0)
	s_setprio 1
	v_mfma_f32_16x16x128_f8f6f4 v[18:21], v[166:169], v[182:185], v[18:21] cbsz:4 blgp:4
	v_mfma_f32_16x16x128_f8f6f4 v[18:21], v[174:177], v[190:193], v[18:21] cbsz:4 blgp:4
	v_mfma_f32_16x16x128_f8f6f4 v[22:25], v[170:173], v[182:185], v[22:25] cbsz:4 blgp:4
	v_mfma_f32_16x16x128_f8f6f4 v[22:25], v[178:181], v[190:193], v[22:25] cbsz:4 blgp:4
	v_mfma_f32_16x16x128_f8f6f4 v[50:53], v[214:217], v[182:185], v[50:53] cbsz:4 blgp:4
	v_mfma_f32_16x16x128_f8f6f4 v[50:53], v[222:225], v[190:193], v[50:53] cbsz:4 blgp:4
	v_mfma_f32_16x16x128_f8f6f4 v[54:57], v[218:221], v[182:185], v[54:57] cbsz:4 blgp:4
	v_mfma_f32_16x16x128_f8f6f4 v[54:57], v[226:229], v[190:193], v[54:57] cbsz:4 blgp:4
	v_mfma_f32_16x16x128_f8f6f4 v[26:29], v[166:169], v[186:189], v[26:29] cbsz:4 blgp:4
	v_mfma_f32_16x16x128_f8f6f4 v[26:29], v[174:177], v[194:197], v[26:29] cbsz:4 blgp:4
	v_mfma_f32_16x16x128_f8f6f4 v[30:33], v[170:173], v[186:189], v[30:33] cbsz:4 blgp:4
	v_mfma_f32_16x16x128_f8f6f4 v[30:33], v[178:181], v[194:197], v[30:33] cbsz:4 blgp:4
	v_mfma_f32_16x16x128_f8f6f4 v[58:61], v[214:217], v[186:189], v[58:61] cbsz:4 blgp:4
	v_mfma_f32_16x16x128_f8f6f4 v[58:61], v[222:225], v[194:197], v[58:61] cbsz:4 blgp:4
	v_mfma_f32_16x16x128_f8f6f4 v[62:65], v[218:221], v[186:189], v[62:65] cbsz:4 blgp:4
	v_mfma_f32_16x16x128_f8f6f4 v[62:65], v[226:229], v[194:197], v[62:65] cbsz:4 blgp:4
	v_mfma_f32_16x16x128_f8f6f4 v[34:37], v[166:169], v[198:201], v[34:37] cbsz:4 blgp:4
	v_mfma_f32_16x16x128_f8f6f4 v[34:37], v[174:177], v[206:209], v[34:37] cbsz:4 blgp:4
	v_mfma_f32_16x16x128_f8f6f4 v[38:41], v[170:173], v[198:201], v[38:41] cbsz:4 blgp:4
	v_mfma_f32_16x16x128_f8f6f4 v[38:41], v[178:181], v[206:209], v[38:41] cbsz:4 blgp:4
	v_mfma_f32_16x16x128_f8f6f4 v[66:69], v[214:217], v[198:201], v[66:69] cbsz:4 blgp:4
	v_mfma_f32_16x16x128_f8f6f4 v[66:69], v[222:225], v[206:209], v[66:69] cbsz:4 blgp:4
	v_mfma_f32_16x16x128_f8f6f4 v[70:73], v[218:221], v[198:201], v[70:73] cbsz:4 blgp:4
	v_mfma_f32_16x16x128_f8f6f4 v[70:73], v[226:229], v[206:209], v[70:73] cbsz:4 blgp:4
	v_mfma_f32_16x16x128_f8f6f4 v[42:45], v[166:169], v[202:205], v[42:45] cbsz:4 blgp:4
	v_mfma_f32_16x16x128_f8f6f4 v[42:45], v[174:177], v[210:213], v[42:45] cbsz:4 blgp:4
	v_mfma_f32_16x16x128_f8f6f4 v[46:49], v[170:173], v[202:205], v[46:49] cbsz:4 blgp:4
	v_mfma_f32_16x16x128_f8f6f4 v[46:49], v[178:181], v[210:213], v[46:49] cbsz:4 blgp:4
	v_mfma_f32_16x16x128_f8f6f4 v[74:77], v[214:217], v[202:205], v[74:77] cbsz:4 blgp:4
	v_mfma_f32_16x16x128_f8f6f4 v[74:77], v[222:225], v[210:213], v[74:77] cbsz:4 blgp:4
	v_mfma_f32_16x16x128_f8f6f4 v[78:81], v[218:221], v[202:205], v[78:81] cbsz:4 blgp:4
	v_mfma_f32_16x16x128_f8f6f4 v[78:81], v[226:229], v[210:213], v[78:81] cbsz:4 blgp:4
	s_setprio 0
	s_barrier
	s_mov_b32 m0, s64
	s_nop 0
	global_load_lds_dwordx4 v148, s[42:43]
	s_mov_b32 m0, s65
	s_nop 0
	global_load_lds_dwordx4 v152, s[42:43]
	ds_read_b128 v[182:185], v163 offset:49152
	ds_read_b128 v[186:189], v163 offset:51200
	ds_read_b128 v[190:193], v164 offset:49152
	ds_read_b128 v[194:197], v164 offset:51200
	ds_read_b128 v[198:201], v163 offset:53248
	ds_read_b128 v[202:205], v163 offset:55296
	ds_read_b128 v[206:209], v164 offset:53248
	ds_read_b128 v[210:213], v164 offset:55296
	s_mov_b32 m0, s66
	s_nop 0
	global_load_lds_dwordx4 v146, s[44:45]
	s_mov_b32 m0, s67
	s_nop 0
	global_load_lds_dwordx4 v150, s[44:45]
	s_add_u32 s42, s42, s24
	s_addc_u32 s43, s43, s25
	s_mov_b32 m0, s68
	s_nop 0
	global_load_lds_dwordx4 v148, s[42:43]
	s_mov_b32 m0, s69
	s_nop 0
	global_load_lds_dwordx4 v152, s[42:43]
	s_waitcnt vmcnt(8)
	s_waitcnt lgkmcnt(0)
	s_barrier
	s_setprio 1
	v_mfma_f32_16x16x128_f8f6f4 v[86:89], v[166:169], v[182:185], v[86:89] cbsz:4 blgp:4
	v_mfma_f32_16x16x128_f8f6f4 v[86:89], v[174:177], v[190:193], v[86:89] cbsz:4 blgp:4
	v_mfma_f32_16x16x128_f8f6f4 v[90:93], v[170:173], v[182:185], v[90:93] cbsz:4 blgp:4
	v_mfma_f32_16x16x128_f8f6f4 v[90:93], v[178:181], v[190:193], v[90:93] cbsz:4 blgp:4
	v_mfma_f32_16x16x128_f8f6f4 v[94:97], v[214:217], v[182:185], v[94:97] cbsz:4 blgp:4
	v_mfma_f32_16x16x128_f8f6f4 v[94:97], v[222:225], v[190:193], v[94:97] cbsz:4 blgp:4
	v_mfma_f32_16x16x128_f8f6f4 v[102:105], v[218:221], v[182:185], v[102:105] cbsz:4 blgp:4
	v_mfma_f32_16x16x128_f8f6f4 v[102:105], v[226:229], v[190:193], v[102:105] cbsz:4 blgp:4
	v_mfma_f32_16x16x128_f8f6f4 v[98:101], v[166:169], v[186:189], v[98:101] cbsz:4 blgp:4
	v_mfma_f32_16x16x128_f8f6f4 v[98:101], v[174:177], v[194:197], v[98:101] cbsz:4 blgp:4
	v_mfma_f32_16x16x128_f8f6f4 v[106:109], v[170:173], v[186:189], v[106:109] cbsz:4 blgp:4
	v_mfma_f32_16x16x128_f8f6f4 v[106:109], v[178:181], v[194:197], v[106:109] cbsz:4 blgp:4
	v_mfma_f32_16x16x128_f8f6f4 v[110:113], v[214:217], v[186:189], v[110:113] cbsz:4 blgp:4
	v_mfma_f32_16x16x128_f8f6f4 v[110:113], v[222:225], v[194:197], v[110:113] cbsz:4 blgp:4
	v_mfma_f32_16x16x128_f8f6f4 v[114:117], v[218:221], v[186:189], v[114:117] cbsz:4 blgp:4
	v_mfma_f32_16x16x128_f8f6f4 v[114:117], v[226:229], v[194:197], v[114:117] cbsz:4 blgp:4
	v_mfma_f32_16x16x128_f8f6f4 v[118:121], v[166:169], v[198:201], v[118:121] cbsz:4 blgp:4
	v_mfma_f32_16x16x128_f8f6f4 v[118:121], v[174:177], v[206:209], v[118:121] cbsz:4 blgp:4
	v_mfma_f32_16x16x128_f8f6f4 v[126:129], v[170:173], v[198:201], v[126:129] cbsz:4 blgp:4
	v_mfma_f32_16x16x128_f8f6f4 v[126:129], v[178:181], v[206:209], v[126:129] cbsz:4 blgp:4
	v_mfma_f32_16x16x128_f8f6f4 v[122:125], v[214:217], v[198:201], v[122:125] cbsz:4 blgp:4
	v_mfma_f32_16x16x128_f8f6f4 v[122:125], v[222:225], v[206:209], v[122:125] cbsz:4 blgp:4
	v_mfma_f32_16x16x128_f8f6f4 v[130:133], v[218:221], v[198:201], v[130:133] cbsz:4 blgp:4
	v_mfma_f32_16x16x128_f8f6f4 v[130:133], v[226:229], v[206:209], v[130:133] cbsz:4 blgp:4
	v_mfma_f32_16x16x128_f8f6f4 v[138:141], v[166:169], v[202:205], v[138:141] cbsz:4 blgp:4
	v_mfma_f32_16x16x128_f8f6f4 v[138:141], v[174:177], v[210:213], v[138:141] cbsz:4 blgp:4
	v_mfma_f32_16x16x128_f8f6f4 v[82:85], v[170:173], v[202:205], v[82:85] cbsz:4 blgp:4
	v_mfma_f32_16x16x128_f8f6f4 v[82:85], v[178:181], v[210:213], v[82:85] cbsz:4 blgp:4
	v_mfma_f32_16x16x128_f8f6f4 v[134:137], v[214:217], v[202:205], v[134:137] cbsz:4 blgp:4
	v_mfma_f32_16x16x128_f8f6f4 v[134:137], v[222:225], v[210:213], v[134:137] cbsz:4 blgp:4
	v_mfma_f32_16x16x128_f8f6f4 v[142:145], v[218:221], v[202:205], v[142:145] cbsz:4 blgp:4
	v_mfma_f32_16x16x128_f8f6f4 v[142:145], v[226:229], v[210:213], v[142:145] cbsz:4 blgp:4
	s_setprio 0
	s_andn2_b64 vcc, exec, s[34:35]
	s_barrier
	s_cbranch_vccnz .LBB4_4
	s_ashr_i32 s29, s28, 31
	s_lshl_b64 s[42:43], s[28:29], 10
	s_add_u32 s42, s10, s42
	s_addc_u32 s43, s11, s43
	s_add_u32 s29, s40, 0x200
	s_addc_u32 s78, s41, 0
	s_add_u32 s79, s38, 0x200
	s_addc_u32 s80, s39, 0
	s_add_u32 s38, s81, 0x180
	s_addc_u32 s39, s82, 0
	s_mov_b32 s81, 4
	s_cmp_eq_u32 s63, s81
	s_cselect_b64 s[40:41], -1, 0
	s_cmp_lg_u32 s63, s81
	s_cbranch_scc1 .LBB4_15

.Lrs_a_5:
	s_add_u32 s82, s42, s22
	s_addc_u32 s83, s43, s23
	s_add_u32 s29, s42, 0x100
	s_addc_u32 s46, s43, 0
	s_and_b64 s[44:45], s[14:15], exec
	ds_read_b128 v[82:85], v163
	ds_read_b128 v[94:97], v163 offset:2048
	ds_read_b128 v[102:105], v164
	ds_read_b128 v[110:113], v164 offset:2048
	s_cselect_b32 s49, s39, s46
	s_cselect_b32 s48, s38, s29
	s_add_u32 s29, s40, 0x100
	s_addc_u32 s46, s41, 0
	s_and_b64 s[44:45], s[14:15], exec
	s_cselect_b32 s51, s5, s46
	s_cselect_b32 s50, s4, s29
	s_add_u32 s46, s48, 0x80
	s_addc_u32 s47, s49, 0
	s_add_u32 s44, s50, 0x80
	s_addc_u32 s45, s51, 0
	ds_read_b128 v[58:61], v165
	ds_read_b128 v[66:69], v165 offset:2048
	ds_read_b128 v[62:65], v166
	ds_read_b128 v[70:73], v166 offset:2048
	ds_read_b128 v[74:77], v165 offset:4096
	ds_read_b128 v[86:89], v165 offset:6144
	ds_read_b128 v[78:81], v166 offset:4096
	ds_read_b128 v[90:93], v166 offset:6144
	s_add_u32 s80, s82, 0x80
	s_addc_u32 s81, s83, 0
	s_mov_b32 m0, s71
	s_nop 0
	global_load_lds_dwordx4 v146, s[80:81]
	s_mov_b32 m0, s72
	s_nop 0
	global_load_lds_dwordx4 v150, s[80:81]
	s_waitcnt lgkmcnt(8)
	ds_read_b128 v[142:145], v163 offset:16384
	ds_read_b128 v[156:159], v163 offset:18432
	ds_read_b128 v[168:171], v164 offset:16384
	ds_read_b128 v[172:175], v164 offset:18432
	s_waitcnt vmcnt(16)
	v_mov_b32_e32 v1, v0
	v_pk_mul_f32 v[16:17], v[0:1], v[16:17]
	v_pk_mul_f32 v[14:15], v[154:155], v[14:15]
	v_pk_mul_f32 v[12:13], v[0:1], v[12:13]
	v_pk_mul_f32 v[10:11], v[154:155], v[10:11]
	v_pk_mul_f32 v[8:9], v[0:1], v[8:9]
	v_pk_mul_f32 v[6:7], v[154:155], v[6:7]
	v_pk_mul_f32 v[4:5], v[0:1], v[4:5]
	v_pk_mul_f32 v[2:3], v[154:155], v[2:3]
	s_waitcnt vmcnt(8)
	s_waitcnt lgkmcnt(0)
	s_barrier
	s_waitcnt lgkmcnt(0)
	s_setprio 1
	v_mfma_f32_16x16x128_f8f6f4 v[18:21], v[82:85], v[58:61], v[14:17] cbsz:4 blgp:4
	v_mfma_f32_16x16x128_f8f6f4 v[18:21], v[102:105], v[62:65], v[18:21] cbsz:4 blgp:4
	v_mfma_f32_16x16x128_f8f6f4 v[22:25], v[94:97], v[58:61], v[10:13] cbsz:4 blgp:4
	v_mfma_f32_16x16x128_f8f6f4 v[22:25], v[110:113], v[62:65], v[22:25] cbsz:4 blgp:4
	v_mfma_f32_16x16x128_f8f6f4 v[50:53], v[142:145], v[58:61], v[6:9] cbsz:4 blgp:4
	v_mfma_f32_16x16x128_f8f6f4 v[50:53], v[168:171], v[62:65], v[50:53] cbsz:4 blgp:4
	v_mfma_f32_16x16x128_f8f6f4 v[54:57], v[156:159], v[58:61], v[2:5] cbsz:4 blgp:4
	v_mfma_f32_16x16x128_f8f6f4 v[54:57], v[172:175], v[62:65], v[54:57] cbsz:4 blgp:4
	v_mfma_f32_16x16x128_f8f6f4 v[26:29], v[82:85], v[66:69], v[14:17] cbsz:4 blgp:4
	v_mfma_f32_16x16x128_f8f6f4 v[26:29], v[102:105], v[70:73], v[26:29] cbsz:4 blgp:4
	v_mfma_f32_16x16x128_f8f6f4 v[30:33], v[94:97], v[66:69], v[10:13] cbsz:4 blgp:4
	v_mfma_f32_16x16x128_f8f6f4 v[30:33], v[110:113], v[70:73], v[30:33] cbsz:4 blgp:4
	v_mfma_f32_16x16x128_f8f6f4 v[58:61], v[142:145], v[66:69], v[6:9] cbsz:4 blgp:4
	v_mfma_f32_16x16x128_f8f6f4 v[58:61], v[168:171], v[70:73], v[58:61] cbsz:4 blgp:4
	v_mfma_f32_16x16x128_f8f6f4 v[62:65], v[156:159], v[66:69], v[2:5] cbsz:4 blgp:4
	v_mfma_f32_16x16x128_f8f6f4 v[62:65], v[172:175], v[70:73], v[62:65] cbsz:4 blgp:4
	v_mfma_f32_16x16x128_f8f6f4 v[34:37], v[82:85], v[74:77], v[14:17] cbsz:4 blgp:4
	v_mfma_f32_16x16x128_f8f6f4 v[34:37], v[102:105], v[78:81], v[34:37] cbsz:4 blgp:4
	v_mfma_f32_16x16x128_f8f6f4 v[38:41], v[94:97], v[74:77], v[10:13] cbsz:4 blgp:4
	v_mfma_f32_16x16x128_f8f6f4 v[38:41], v[110:113], v[78:81], v[38:41] cbsz:4 blgp:4
	v_mfma_f32_16x16x128_f8f6f4 v[66:69], v[142:145], v[74:77], v[6:9] cbsz:4 blgp:4
	v_mfma_f32_16x16x128_f8f6f4 v[66:69], v[168:171], v[78:81], v[66:69] cbsz:4 blgp:4
	v_mfma_f32_16x16x128_f8f6f4 v[70:73], v[156:159], v[74:77], v[2:5] cbsz:4 blgp:4
	v_mfma_f32_16x16x128_f8f6f4 v[70:73], v[172:175], v[78:81], v[70:73] cbsz:4 blgp:4
	v_mfma_f32_16x16x128_f8f6f4 v[42:45], v[82:85], v[86:89], v[14:17] cbsz:4 blgp:4
	v_mfma_f32_16x16x128_f8f6f4 v[42:45], v[102:105], v[90:93], v[42:45] cbsz:4 blgp:4
	v_mfma_f32_16x16x128_f8f6f4 v[46:49], v[94:97], v[86:89], v[10:13] cbsz:4 blgp:4
	v_mfma_f32_16x16x128_f8f6f4 v[46:49], v[110:113], v[90:93], v[46:49] cbsz:4 blgp:4
	v_mfma_f32_16x16x128_f8f6f4 v[74:77], v[142:145], v[86:89], v[6:9] cbsz:4 blgp:4
	v_mfma_f32_16x16x128_f8f6f4 v[74:77], v[168:171], v[90:93], v[74:77] cbsz:4 blgp:4
	v_mfma_f32_16x16x128_f8f6f4 v[78:81], v[156:159], v[86:89], v[2:5] cbsz:4 blgp:4
	v_mfma_f32_16x16x128_f8f6f4 v[78:81], v[172:175], v[90:93], v[78:81] cbsz:4 blgp:4
	s_setprio 0
	s_barrier
	s_mov_b32 m0, s56
	s_nop 0
	global_load_lds_dwordx4 v148, s[50:51]
	s_mov_b32 m0, s57
	s_nop 0
	global_load_lds_dwordx4 v152, s[50:51]
	ds_read_b128 v[114:117], v165 offset:16384
	ds_read_b128 v[122:125], v165 offset:18432
	ds_read_b128 v[130:133], v166 offset:16384
	ds_read_b128 v[134:137], v166 offset:18432
	ds_read_b128 v[176:179], v165 offset:20480
	ds_read_b128 v[180:183], v165 offset:22528
	ds_read_b128 v[184:187], v166 offset:20480
	ds_read_b128 v[188:191], v166 offset:22528
	s_mov_b32 m0, s55
	s_nop 0
	global_load_lds_dwordx4 v146, s[48:49]
	s_mov_b32 m0, s58
	s_nop 0
	global_load_lds_dwordx4 v150, s[48:49]
	s_add_u32 s50, s50, s24
	s_addc_u32 s51, s51, s25
	s_mov_b32 m0, s59
	s_nop 0
	global_load_lds_dwordx4 v148, s[50:51]
	s_mov_b32 m0, s60
	s_nop 0
	global_load_lds_dwordx4 v152, s[50:51]
	s_waitcnt vmcnt(8)
	s_waitcnt lgkmcnt(0)
	s_barrier
	s_setprio 1
	v_mfma_f32_16x16x128_f8f6f4 v[86:89], v[82:85], v[114:117], v[14:17] cbsz:4 blgp:4
	v_mfma_f32_16x16x128_f8f6f4 v[86:89], v[102:105], v[130:133], v[86:89] cbsz:4 blgp:4
	v_mfma_f32_16x16x128_f8f6f4 v[90:93], v[94:97], v[114:117], v[10:13] cbsz:4 blgp:4
	v_mfma_f32_16x16x128_f8f6f4 v[90:93], v[110:113], v[130:133], v[90:93] cbsz:4 blgp:4
	v_mfma_f32_16x16x128_f8f6f4 v[98:101], v[82:85], v[122:125], v[14:17] cbsz:4 blgp:4
	v_mfma_f32_16x16x128_f8f6f4 v[98:101], v[102:105], v[134:137], v[98:101] cbsz:4 blgp:4
	v_mfma_f32_16x16x128_f8f6f4 v[106:109], v[94:97], v[122:125], v[10:13] cbsz:4 blgp:4
	v_mfma_f32_16x16x128_f8f6f4 v[106:109], v[110:113], v[134:137], v[106:109] cbsz:4 blgp:4
	v_mfma_f32_16x16x128_f8f6f4 v[118:121], v[82:85], v[176:179], v[14:17] cbsz:4 blgp:4
	v_mfma_f32_16x16x128_f8f6f4 v[118:121], v[102:105], v[184:187], v[118:121] cbsz:4 blgp:4
	v_mfma_f32_16x16x128_f8f6f4 v[126:129], v[94:97], v[176:179], v[10:13] cbsz:4 blgp:4
	v_mfma_f32_16x16x128_f8f6f4 v[126:129], v[110:113], v[184:187], v[126:129] cbsz:4 blgp:4
	v_mfma_f32_16x16x128_f8f6f4 v[138:141], v[82:85], v[180:183], v[14:17] cbsz:4 blgp:4
	v_mfma_f32_16x16x128_f8f6f4 v[138:141], v[102:105], v[188:191], v[138:141] cbsz:4 blgp:4
	v_mfma_f32_16x16x128_f8f6f4 v[82:85], v[94:97], v[180:183], v[10:13] cbsz:4 blgp:4
	v_mfma_f32_16x16x128_f8f6f4 v[82:85], v[110:113], v[188:191], v[82:85] cbsz:4 blgp:4
	v_mfma_f32_16x16x128_f8f6f4 v[94:97], v[142:145], v[114:117], v[6:9] cbsz:4 blgp:4
	v_mfma_f32_16x16x128_f8f6f4 v[94:97], v[168:171], v[130:133], v[94:97] cbsz:4 blgp:4
	v_mfma_f32_16x16x128_f8f6f4 v[102:105], v[156:159], v[114:117], v[2:5] cbsz:4 blgp:4
	v_mfma_f32_16x16x128_f8f6f4 v[102:105], v[172:175], v[130:133], v[102:105] cbsz:4 blgp:4
	v_mfma_f32_16x16x128_f8f6f4 v[110:113], v[142:145], v[122:125], v[6:9] cbsz:4 blgp:4
	v_mfma_f32_16x16x128_f8f6f4 v[110:113], v[168:171], v[134:137], v[110:113] cbsz:4 blgp:4
	v_mfma_f32_16x16x128_f8f6f4 v[114:117], v[156:159], v[122:125], v[2:5] cbsz:4 blgp:4
	v_mfma_f32_16x16x128_f8f6f4 v[114:117], v[172:175], v[134:137], v[114:117] cbsz:4 blgp:4
	v_mfma_f32_16x16x128_f8f6f4 v[122:125], v[142:145], v[176:179], v[6:9] cbsz:4 blgp:4
	v_mfma_f32_16x16x128_f8f6f4 v[122:125], v[168:171], v[184:187], v[122:125] cbsz:4 blgp:4
	v_mfma_f32_16x16x128_f8f6f4 v[130:133], v[156:159], v[176:179], v[2:5] cbsz:4 blgp:4
	v_mfma_f32_16x16x128_f8f6f4 v[130:133], v[172:175], v[184:187], v[130:133] cbsz:4 blgp:4
	v_mfma_f32_16x16x128_f8f6f4 v[134:137], v[142:145], v[180:183], v[6:9] cbsz:4 blgp:4
	v_mfma_f32_16x16x128_f8f6f4 v[134:137], v[168:171], v[188:191], v[134:137] cbsz:4 blgp:4
	v_mfma_f32_16x16x128_f8f6f4 v[142:145], v[156:159], v[180:183], v[2:5] cbsz:4 blgp:4
	v_mfma_f32_16x16x128_f8f6f4 v[142:145], v[172:175], v[188:191], v[142:145] cbsz:4 blgp:4
	s_setprio 0
	s_barrier
	ds_read_b128 v[156:159], v163 offset:32768
	ds_read_b128 v[168:171], v163 offset:34816
	ds_read_b128 v[172:175], v164 offset:32768
	ds_read_b128 v[176:179], v164 offset:34816
	ds_read_b128 v[180:183], v165 offset:32768
	ds_read_b128 v[184:187], v165 offset:34816
	ds_read_b128 v[188:191], v166 offset:32768
	ds_read_b128 v[192:195], v166 offset:34816
	ds_read_b128 v[196:199], v165 offset:36864
	ds_read_b128 v[200:203], v165 offset:38912
	ds_read_b128 v[204:207], v166 offset:36864
	ds_read_b128 v[208:211], v166 offset:38912
	s_add_u32 s48, s48, s22
	s_addc_u32 s49, s49, s23
	s_mov_b32 m0, s61
	s_nop 0
	global_load_lds_dwordx4 v146, s[48:49]
	s_mov_b32 m0, s62
	s_nop 0
	global_load_lds_dwordx4 v150, s[48:49]
	s_waitcnt lgkmcnt(8)
	ds_read_b128 v[212:215], v163 offset:49152
	ds_read_b128 v[216:219], v163 offset:51200
	ds_read_b128 v[220:223], v164 offset:49152
	ds_read_b128 v[224:227], v164 offset:51200
	s_waitcnt vmcnt(8)
	s_waitcnt lgkmcnt(0)
	s_barrier
	s_waitcnt lgkmcnt(0)
	s_setprio 1
	v_mfma_f32_16x16x128_f8f6f4 v[18:21], v[156:159], v[180:183], v[18:21] cbsz:4 blgp:4
	v_mfma_f32_16x16x128_f8f6f4 v[18:21], v[172:175], v[188:191], v[18:21] cbsz:4 blgp:4
	v_mfma_f32_16x16x128_f8f6f4 v[22:25], v[168:171], v[180:183], v[22:25] cbsz:4 blgp:4
	v_mfma_f32_16x16x128_f8f6f4 v[22:25], v[176:179], v[188:191], v[22:25] cbsz:4 blgp:4
	v_mfma_f32_16x16x128_f8f6f4 v[50:53], v[212:215], v[180:183], v[50:53] cbsz:4 blgp:4
	v_mfma_f32_16x16x128_f8f6f4 v[50:53], v[220:223], v[188:191], v[50:53] cbsz:4 blgp:4
	v_mfma_f32_16x16x128_f8f6f4 v[54:57], v[216:219], v[180:183], v[54:57] cbsz:4 blgp:4
	v_mfma_f32_16x16x128_f8f6f4 v[54:57], v[224:227], v[188:191], v[54:57] cbsz:4 blgp:4
	v_mfma_f32_16x16x128_f8f6f4 v[26:29], v[156:159], v[184:187], v[26:29] cbsz:4 blgp:4
	v_mfma_f32_16x16x128_f8f6f4 v[26:29], v[172:175], v[192:195], v[26:29] cbsz:4 blgp:4
	v_mfma_f32_16x16x128_f8f6f4 v[30:33], v[168:171], v[184:187], v[30:33] cbsz:4 blgp:4
	v_mfma_f32_16x16x128_f8f6f4 v[30:33], v[176:179], v[192:195], v[30:33] cbsz:4 blgp:4
	v_mfma_f32_16x16x128_f8f6f4 v[58:61], v[212:215], v[184:187], v[58:61] cbsz:4 blgp:4
	v_mfma_f32_16x16x128_f8f6f4 v[58:61], v[220:223], v[192:195], v[58:61] cbsz:4 blgp:4
	v_mfma_f32_16x16x128_f8f6f4 v[62:65], v[216:219], v[184:187], v[62:65] cbsz:4 blgp:4
	v_mfma_f32_16x16x128_f8f6f4 v[62:65], v[224:227], v[192:195], v[62:65] cbsz:4 blgp:4
	v_mfma_f32_16x16x128_f8f6f4 v[34:37], v[156:159], v[196:199], v[34:37] cbsz:4 blgp:4
	v_mfma_f32_16x16x128_f8f6f4 v[34:37], v[172:175], v[204:207], v[34:37] cbsz:4 blgp:4
	v_mfma_f32_16x16x128_f8f6f4 v[38:41], v[168:171], v[196:199], v[38:41] cbsz:4 blgp:4
	v_mfma_f32_16x16x128_f8f6f4 v[38:41], v[176:179], v[204:207], v[38:41] cbsz:4 blgp:4
	v_mfma_f32_16x16x128_f8f6f4 v[66:69], v[212:215], v[196:199], v[66:69] cbsz:4 blgp:4
	v_mfma_f32_16x16x128_f8f6f4 v[66:69], v[220:223], v[204:207], v[66:69] cbsz:4 blgp:4
	v_mfma_f32_16x16x128_f8f6f4 v[70:73], v[216:219], v[196:199], v[70:73] cbsz:4 blgp:4
	v_mfma_f32_16x16x128_f8f6f4 v[70:73], v[224:227], v[204:207], v[70:73] cbsz:4 blgp:4
	v_mfma_f32_16x16x128_f8f6f4 v[42:45], v[156:159], v[200:203], v[42:45] cbsz:4 blgp:4
	v_mfma_f32_16x16x128_f8f6f4 v[42:45], v[172:175], v[208:211], v[42:45] cbsz:4 blgp:4
	v_mfma_f32_16x16x128_f8f6f4 v[46:49], v[168:171], v[200:203], v[46:49] cbsz:4 blgp:4
	v_mfma_f32_16x16x128_f8f6f4 v[46:49], v[176:179], v[208:211], v[46:49] cbsz:4 blgp:4
	v_mfma_f32_16x16x128_f8f6f4 v[74:77], v[212:215], v[200:203], v[74:77] cbsz:4 blgp:4
	v_mfma_f32_16x16x128_f8f6f4 v[74:77], v[220:223], v[208:211], v[74:77] cbsz:4 blgp:4
	v_mfma_f32_16x16x128_f8f6f4 v[78:81], v[216:219], v[200:203], v[78:81] cbsz:4 blgp:4
	v_mfma_f32_16x16x128_f8f6f4 v[78:81], v[224:227], v[208:211], v[78:81] cbsz:4 blgp:4
	s_setprio 0
	s_barrier
	s_mov_b32 m0, s65
	s_nop 0
	global_load_lds_dwordx4 v148, s[44:45]
	s_mov_b32 m0, s66
	s_nop 0
	global_load_lds_dwordx4 v152, s[44:45]
	ds_read_b128 v[180:183], v165 offset:49152
	ds_read_b128 v[184:187], v165 offset:51200
	ds_read_b128 v[188:191], v166 offset:49152
	ds_read_b128 v[192:195], v166 offset:51200
	ds_read_b128 v[196:199], v165 offset:53248
	ds_read_b128 v[200:203], v165 offset:55296
	ds_read_b128 v[204:207], v166 offset:53248
	ds_read_b128 v[208:211], v166 offset:55296
	s_mov_b32 m0, s67
	s_nop 0
	global_load_lds_dwordx4 v146, s[46:47]
	s_mov_b32 m0, s68
	s_nop 0
	global_load_lds_dwordx4 v150, s[46:47]
	s_add_u32 s44, s44, s24
	s_addc_u32 s45, s45, s25
	s_mov_b32 m0, s69
	s_nop 0
	global_load_lds_dwordx4 v148, s[44:45]
	s_mov_b32 m0, s70
	s_nop 0
	global_load_lds_dwordx4 v152, s[44:45]
	s_waitcnt vmcnt(8)
	s_waitcnt lgkmcnt(0)
	s_barrier
	s_setprio 1
	v_mfma_f32_16x16x128_f8f6f4 v[86:89], v[156:159], v[180:183], v[86:89] cbsz:4 blgp:4
	v_mfma_f32_16x16x128_f8f6f4 v[86:89], v[172:175], v[188:191], v[86:89] cbsz:4 blgp:4
	v_mfma_f32_16x16x128_f8f6f4 v[90:93], v[168:171], v[180:183], v[90:93] cbsz:4 blgp:4
	v_mfma_f32_16x16x128_f8f6f4 v[90:93], v[176:179], v[188:191], v[90:93] cbsz:4 blgp:4
	v_mfma_f32_16x16x128_f8f6f4 v[94:97], v[212:215], v[180:183], v[94:97] cbsz:4 blgp:4
	v_mfma_f32_16x16x128_f8f6f4 v[94:97], v[220:223], v[188:191], v[94:97] cbsz:4 blgp:4
	v_mfma_f32_16x16x128_f8f6f4 v[102:105], v[216:219], v[180:183], v[102:105] cbsz:4 blgp:4
	v_mfma_f32_16x16x128_f8f6f4 v[102:105], v[224:227], v[188:191], v[102:105] cbsz:4 blgp:4
	v_mfma_f32_16x16x128_f8f6f4 v[98:101], v[156:159], v[184:187], v[98:101] cbsz:4 blgp:4
	v_mfma_f32_16x16x128_f8f6f4 v[98:101], v[172:175], v[192:195], v[98:101] cbsz:4 blgp:4
	v_mfma_f32_16x16x128_f8f6f4 v[106:109], v[168:171], v[184:187], v[106:109] cbsz:4 blgp:4
	v_mfma_f32_16x16x128_f8f6f4 v[106:109], v[176:179], v[192:195], v[106:109] cbsz:4 blgp:4
	v_mfma_f32_16x16x128_f8f6f4 v[110:113], v[212:215], v[184:187], v[110:113] cbsz:4 blgp:4
	v_mfma_f32_16x16x128_f8f6f4 v[110:113], v[220:223], v[192:195], v[110:113] cbsz:4 blgp:4
	v_mfma_f32_16x16x128_f8f6f4 v[114:117], v[216:219], v[184:187], v[114:117] cbsz:4 blgp:4
	v_mfma_f32_16x16x128_f8f6f4 v[114:117], v[224:227], v[192:195], v[114:117] cbsz:4 blgp:4
	v_mfma_f32_16x16x128_f8f6f4 v[118:121], v[156:159], v[196:199], v[118:121] cbsz:4 blgp:4
	v_mfma_f32_16x16x128_f8f6f4 v[118:121], v[172:175], v[204:207], v[118:121] cbsz:4 blgp:4
	v_mfma_f32_16x16x128_f8f6f4 v[126:129], v[168:171], v[196:199], v[126:129] cbsz:4 blgp:4
	v_mfma_f32_16x16x128_f8f6f4 v[126:129], v[176:179], v[204:207], v[126:129] cbsz:4 blgp:4
	v_mfma_f32_16x16x128_f8f6f4 v[122:125], v[212:215], v[196:199], v[122:125] cbsz:4 blgp:4
	v_mfma_f32_16x16x128_f8f6f4 v[122:125], v[220:223], v[204:207], v[122:125] cbsz:4 blgp:4
	v_mfma_f32_16x16x128_f8f6f4 v[130:133], v[216:219], v[196:199], v[130:133] cbsz:4 blgp:4
	v_mfma_f32_16x16x128_f8f6f4 v[130:133], v[224:227], v[204:207], v[130:133] cbsz:4 blgp:4
	v_mfma_f32_16x16x128_f8f6f4 v[138:141], v[156:159], v[200:203], v[138:141] cbsz:4 blgp:4
	v_mfma_f32_16x16x128_f8f6f4 v[138:141], v[172:175], v[208:211], v[138:141] cbsz:4 blgp:4
	v_mfma_f32_16x16x128_f8f6f4 v[82:85], v[168:171], v[200:203], v[82:85] cbsz:4 blgp:4
	v_mfma_f32_16x16x128_f8f6f4 v[82:85], v[176:179], v[208:211], v[82:85] cbsz:4 blgp:4
	v_mfma_f32_16x16x128_f8f6f4 v[134:137], v[212:215], v[200:203], v[134:137] cbsz:4 blgp:4
	v_mfma_f32_16x16x128_f8f6f4 v[134:137], v[220:223], v[208:211], v[134:137] cbsz:4 blgp:4
	v_mfma_f32_16x16x128_f8f6f4 v[142:145], v[216:219], v[200:203], v[142:145] cbsz:4 blgp:4
	v_mfma_f32_16x16x128_f8f6f4 v[142:145], v[224:227], v[208:211], v[142:145] cbsz:4 blgp:4
	s_setprio 0
	s_andn2_b64 vcc, exec, s[34:35]
	s_barrier
	s_cbranch_vccnz .LBB5_4
	s_ashr_i32 s29, s28, 31
	s_lshl_b64 s[44:45], s[28:29], 10
	s_add_u32 s44, s10, s44
	s_addc_u32 s45, s11, s45
	s_add_u32 s29, s42, 0x200
	s_addc_u32 s79, s43, 0
	s_add_u32 s80, s40, 0x200
	s_addc_u32 s81, s41, 0
	s_add_u32 s40, s82, 0x180
	s_addc_u32 s41, s83, 0
	s_mov_b32 s82, 4
	s_cmp_eq_u32 s64, s82
	s_cselect_b64 s[42:43], -1, 0
	s_cmp_lg_u32 s64, s82
	s_cbranch_scc1 .LBB5_15
